# v48 + P7 LayerNorm gamma/beta prefetched two tiles ahead with counted waits + P4 unit prologue: the up-to-8 dependent Floc load rounds issued as one batch
# speedup vs baseline: 1.0027x; 1.0027x over previous
.LBB0_626:
	v_mov_b32_e32 v36, v0
	v_cmp_lt_i32_e32 vcc, v184, v185
	v_and_b32_e32 v192, 63, v36
	v_or_b32_e32 v4, s59, v192
	v_ashrrev_i32_e32 v5, 31, v4
	v_lshl_add_u64 v[4:5], v[4:5], 2, s[18:19]
	global_load_dword v4, v[4:5], off
	v_cndmask_b32_e32 v2, v184, v183, vcc
	v_lshlrev_b32_e32 v2, 2, v2
	v_cmp_lt_i32_e32 vcc, v186, v185
	v_cmp_gt_u32_e64 s[10:11], 32, v192
	s_lshl_b32 s49, s48, 8
	v_cndmask_b32_e32 v5, v186, v183, vcc
	v_cmp_eq_u32_e32 vcc, 0, v192
	v_lshlrev_b32_e32 v5, 2, v5
	v_ashrrev_i32_e32 v37, 31, v36
	s_mov_b32 s2, 0
	s_add_i32 s14, s49, 0x100
	s_waitcnt vmcnt(0)
	ds_bpermute_b32 v2, v2, v4
	s_waitcnt lgkmcnt(0)
	v_add_f32_e32 v2, v4, v2
	v_cndmask_b32_e32 v2, v2, v4, vcc
	ds_bpermute_b32 v5, v5, v2
	v_cmp_lt_i32_e32 vcc, v187, v185
	s_waitcnt lgkmcnt(0)
	v_add_f32_e32 v5, v2, v5
	v_cndmask_b32_e32 v6, v187, v183, vcc
	v_cmp_gt_u32_e32 vcc, 2, v192
	v_lshlrev_b32_e32 v6, 2, v6
	s_nop 0
	v_cndmask_b32_e32 v2, v5, v2, vcc
	ds_bpermute_b32 v5, v6, v2
	v_cmp_lt_i32_e32 vcc, v188, v185
	s_waitcnt lgkmcnt(0)
	v_add_f32_e32 v5, v2, v5
	v_cndmask_b32_e32 v6, v188, v183, vcc
	v_cmp_gt_u32_e32 vcc, 4, v192
	v_lshlrev_b32_e32 v6, 2, v6
	s_nop 0
	v_cndmask_b32_e32 v2, v5, v2, vcc
	ds_bpermute_b32 v5, v6, v2
	v_cmp_lt_i32_e32 vcc, v189, v185
	s_waitcnt lgkmcnt(0)
	v_add_f32_e32 v5, v2, v5
	v_cndmask_b32_e32 v6, v189, v183, vcc
	v_cmp_gt_u32_e32 vcc, 8, v192
	v_lshlrev_b32_e32 v6, 2, v6
	s_nop 0
	v_cndmask_b32_e32 v2, v5, v2, vcc
	ds_bpermute_b32 v5, v6, v2
	v_cmp_lt_i32_e32 vcc, v190, v185
	s_waitcnt lgkmcnt(0)
	v_add_f32_e32 v5, v2, v5
	v_cndmask_b32_e32 v6, v190, v183, vcc
	v_cmp_gt_u32_e32 vcc, 16, v192
	v_lshlrev_b32_e32 v6, 2, v6
	s_nop 0
	v_cndmask_b32_e32 v5, v5, v2, vcc
	ds_bpermute_b32 v6, v6, v5
	v_lshl_add_u32 v2, v36, 2, s33
	s_waitcnt lgkmcnt(0)
	v_add_f32_e32 v6, v5, v6
	v_cndmask_b32_e64 v5, v6, v5, s[10:11]
	v_sub_f32_e32 v6, v5, v4
	v_lshl_add_u64 v[4:5], v[36:37], 2, s[42:43]
	v_lshlrev_b32_e32 v8, 2, v36
	v_lshrrev_b32_e32 v12, 6, v36
	global_load_dword v16, v8, s[42:43]
	global_load_dword v17, v8, s[42:43] offset:2048
	v_add_u32_e32 v9, 0x1000, v8
	v_add_u32_e32 v10, 0x2000, v8
	global_load_dword v18, v9, s[42:43]
	global_load_dword v19, v9, s[42:43] offset:2048
	v_add_u32_e32 v11, 0x3000, v8
	global_load_dword v20, v10, s[42:43]
	global_load_dword v21, v10, s[42:43] offset:2048
	global_load_dword v22, v11, s[42:43]
	global_load_dword v23, v11, s[42:43] offset:2048
	v_add_u32_e32 v13, 0, v12
	v_or_b32_e32 v13, v13, v185
	v_lshlrev_b32_e32 v13, 2, v13
	ds_bpermute_b32 v24, v13, v6
	v_add_u32_e32 v14, 8, v12
	v_or_b32_e32 v14, v14, v185
	v_lshlrev_b32_e32 v14, 2, v14
	ds_bpermute_b32 v25, v14, v6
	v_add_u32_e32 v15, 16, v12
	v_or_b32_e32 v15, v15, v185
	v_lshlrev_b32_e32 v15, 2, v15
	ds_bpermute_b32 v26, v15, v6
	v_add_u32_e32 v32, 24, v12
	v_or_b32_e32 v32, v32, v185
	v_lshlrev_b32_e32 v32, 2, v32
	ds_bpermute_b32 v27, v32, v6
	v_add_u32_e32 v33, 32, v12
	v_or_b32_e32 v33, v33, v185
	v_lshlrev_b32_e32 v33, 2, v33
	ds_bpermute_b32 v28, v33, v6
	v_add_u32_e32 v34, 40, v12
	v_or_b32_e32 v34, v34, v185
	v_lshlrev_b32_e32 v34, 2, v34
	ds_bpermute_b32 v29, v34, v6
	v_add_u32_e32 v35, 48, v12
	v_or_b32_e32 v35, v35, v185
	v_lshlrev_b32_e32 v35, 2, v35
	ds_bpermute_b32 v30, v35, v6
	v_add_u32_e32 v4, 56, v12
	v_or_b32_e32 v4, v4, v185
	v_lshlrev_b32_e32 v4, 2, v4
	ds_bpermute_b32 v31, v4, v6
	s_waitcnt vmcnt(0) lgkmcnt(0)
	v_add_f32_e32 v16, v16, v24
	v_mul_f32_e32 v16, 0x3fb8aa3b, v16
	ds_write_b32 v2, v16
	v_add_f32_e32 v17, v17, v25
	v_mul_f32_e32 v17, 0x3fb8aa3b, v17
	ds_write_b32 v2, v17 offset:2048
	v_add_f32_e32 v18, v18, v26
	v_mul_f32_e32 v18, 0x3fb8aa3b, v18
	ds_write_b32 v2, v18 offset:4096
	v_add_f32_e32 v19, v19, v27
	v_mul_f32_e32 v19, 0x3fb8aa3b, v19
	ds_write_b32 v2, v19 offset:6144
	v_add_f32_e32 v20, v20, v28
	v_mul_f32_e32 v20, 0x3fb8aa3b, v20
	ds_write_b32 v2, v20 offset:8192
	v_add_f32_e32 v21, v21, v29
	v_mul_f32_e32 v21, 0x3fb8aa3b, v21
	ds_write_b32 v2, v21 offset:10240
	v_add_f32_e32 v22, v22, v30
	v_mul_f32_e32 v22, 0x3fb8aa3b, v22
	ds_write_b32 v2, v22 offset:12288
	v_add_f32_e32 v23, v23, v31
	v_mul_f32_e32 v23, 0x3fb8aa3b, v23
	ds_write_b32 v2, v23 offset:14336

.LBB0_1048:
	s_or_b64 exec, exec, s[6:7]
	s_waitcnt lgkmcnt(1)
	v_and_b32_e32 v94, 0x78, v106
	v_add_u32_e32 v147, 0, v94
	v_add_u32_e32 v94, 0x20000, v147
	v_add_u32_e32 v96, 0x20200, v147
	v_add_u32_e32 v106, 0x20400, v147
	s_waitcnt lgkmcnt(0)
	s_barrier
	v_add_u32_e32 v108, 0x20600, v147
	ds_read_b64 v[94:95], v94
	ds_read_b64 v[96:97], v96
	ds_read_b64 v[106:107], v106
	ds_read_b64 v[108:109], v108
	v_add_u32_e32 v110, 0x20800, v147
	s_waitcnt lgkmcnt(3)
	v_pk_add_f32 v[94:95], v[94:95], 0 op_sel_hi:[1,0]
	v_add_u32_e32 v111, 0x20a00, v147
	v_add_u32_e32 v112, 0x20c00, v147
	v_add_u32_e32 v113, 0x20e00, v147
	s_waitcnt lgkmcnt(2)
	v_pk_add_f32 v[94:95], v[94:95], v[96:97]
	v_add_u32_e32 v114, 0x20c80, v147
	s_waitcnt lgkmcnt(1)
	v_pk_add_f32 v[94:95], v[94:95], v[106:107]
	ds_read_b64 v[96:97], v110
	ds_read_b64 v[106:107], v111
	ds_read_b64 v[110:111], v112
	ds_read_b64 v[112:113], v113
	s_waitcnt lgkmcnt(4)
	v_pk_add_f32 v[94:95], v[94:95], v[108:109]
	v_add_u32_e32 v108, 0x20480, v147
	s_waitcnt lgkmcnt(3)
	v_pk_add_f32 v[94:95], v[94:95], v[96:97]
	v_add_u32_e32 v115, 0x20e80, v147
	s_waitcnt lgkmcnt(2)
	v_pk_add_f32 v[94:95], v[94:95], v[106:107]
	v_add_u32_e32 v157, 0x20d00, v147
	s_waitcnt lgkmcnt(1)
	v_pk_add_f32 v[94:95], v[94:95], v[110:111]
	v_add_u32_e32 v110, 0x20680, v147
	s_waitcnt lgkmcnt(0)
	v_pk_add_f32 v[94:95], v[94:95], v[112:113]
	v_add_u32_e32 v112, 0x20880, v147
	v_pk_mul_f32 v[94:95], v[94:95], s[72:73] op_sel_hi:[1,0]
	v_add_u32_e32 v113, 0x20a80, v147
	v_fma_f32 v96, -v94, v94, v95
	v_max_f32_e32 v96, 0, v96
	v_add_f32_e32 v96, 0x3727c5ac, v96
	v_mul_f32_e32 v97, 0x4f800000, v96
	v_cmp_gt_f32_e32 vcc, s73, v96
	v_add_u32_e32 v159, 0x20f00, v147
	v_ashrrev_i32_e32 v161, 31, v160
	v_cndmask_b32_e32 v96, v96, v97, vcc
	v_sqrt_f32_e32 v97, v96
	v_lshlrev_b64 v[166:167], 2, v[160:161]
	v_or_b32_e32 v176, s74, v217
	v_ashrrev_i32_e32 v177, 31, v176
	v_add_u32_e32 v106, -1, v97
	v_fma_f32 v107, -v106, v97, v96
	v_cmp_ge_f32_e64 s[6:7], 0, v107
	v_add_u32_e32 v107, 1, v97
	v_pk_add_f32 v[78:79], v[78:79], v[94:95] op_sel_hi:[1,0] neg_lo:[0,1] neg_hi:[0,1]
	v_cndmask_b32_e64 v106, v97, v106, s[6:7]
	v_fma_f32 v97, -v107, v97, v96
	v_cmp_lt_f32_e64 s[6:7], 0, v97
	v_pk_add_f32 v[80:81], v[80:81], v[94:95] op_sel_hi:[1,0] neg_lo:[0,1] neg_hi:[0,1]
	v_pk_add_f32 v[70:71], v[70:71], v[94:95] op_sel_hi:[1,0] neg_lo:[0,1] neg_hi:[0,1]
	v_cndmask_b32_e64 v97, v106, v107, s[6:7]
	v_mul_f32_e32 v106, 0x37800000, v97
	v_cndmask_b32_e32 v97, v97, v106, vcc
	v_cmp_class_f32_e32 vcc, v96, v213
	v_add_u32_e32 v106, 0x20280, v147
	v_pk_add_f32 v[72:73], v[72:73], v[94:95] op_sel_hi:[1,0] neg_lo:[0,1] neg_hi:[0,1]
	v_cndmask_b32_e32 v116, v97, v96, vcc
	v_div_scale_f32 v117, s[6:7], v116, v116, 1.0
	v_rcp_f32_e32 v149, v117
	v_div_scale_f32 v151, vcc, 1.0, v116, 1.0
	v_pk_add_f32 v[62:63], v[62:63], v[94:95] op_sel_hi:[1,0] neg_lo:[0,1] neg_hi:[0,1]
	v_fma_f32 v96, -v117, v149, 1.0
	v_fmac_f32_e32 v149, v96, v149
	v_add_u32_e32 v96, 0x20080, v147
	ds_read_b64 v[96:97], v96
	ds_read_b64 v[106:107], v106
	ds_read_b64 v[108:109], v108
	ds_read_b64 v[110:111], v110
	v_mul_f32_e32 v153, v151, v149
	s_waitcnt lgkmcnt(3)
	v_pk_add_f32 v[96:97], v[96:97], 0 op_sel_hi:[1,0]
	v_pk_add_f32 v[64:65], v[64:65], v[94:95] op_sel_hi:[1,0] neg_lo:[0,1] neg_hi:[0,1]
	s_waitcnt lgkmcnt(2)
	v_pk_add_f32 v[96:97], v[96:97], v[106:107]
	v_pk_add_f32 v[54:55], v[54:55], v[94:95] op_sel_hi:[1,0] neg_lo:[0,1] neg_hi:[0,1]
	s_waitcnt lgkmcnt(1)
	v_pk_add_f32 v[96:97], v[96:97], v[108:109]
	ds_read_b64 v[106:107], v112
	ds_read_b64 v[108:109], v113
	ds_read_b64 v[112:113], v114
	ds_read_b64 v[114:115], v115
	s_waitcnt lgkmcnt(4)
	v_pk_add_f32 v[96:97], v[96:97], v[110:111]
	v_pk_add_f32 v[56:57], v[56:57], v[94:95] op_sel_hi:[1,0] neg_lo:[0,1] neg_hi:[0,1]
	s_waitcnt lgkmcnt(3)
	v_pk_add_f32 v[96:97], v[96:97], v[106:107]
	v_pk_add_f32 v[58:59], v[58:59], v[94:95] op_sel_hi:[1,0] neg_lo:[0,1] neg_hi:[0,1]
	s_waitcnt lgkmcnt(2)
	v_pk_add_f32 v[96:97], v[96:97], v[108:109]
	v_fma_f32 v108, -v117, v153, v151
	s_waitcnt lgkmcnt(1)
	v_pk_add_f32 v[96:97], v[96:97], v[112:113]
	v_fmac_f32_e32 v153, v108, v149
	s_waitcnt lgkmcnt(0)
	v_pk_add_f32 v[96:97], v[96:97], v[114:115]
	v_fma_f32 v108, -v117, v153, v151
	v_pk_mul_f32 v[96:97], v[96:97], s[72:73] op_sel_hi:[1,0]
	v_add_u32_e32 v112, 0x20500, v147
	v_fma_f32 v106, -v96, v96, v97
	v_max_f32_e32 v106, 0, v106
	v_add_f32_e32 v106, 0x3727c5ac, v106
	v_mul_f32_e32 v107, 0x4f800000, v106
	v_cmp_gt_f32_e64 s[6:7], s73, v106
	v_add_u32_e32 v114, 0x20700, v147
	v_add_u32_e32 v117, 0x20b00, v147
	v_cndmask_b32_e64 v106, v106, v107, s[6:7]
	v_sqrt_f32_e32 v107, v106
	v_pk_add_f32 v[60:61], v[60:61], v[94:95] op_sel_hi:[1,0] neg_lo:[0,1] neg_hi:[0,1]
	v_pk_add_f32 v[26:27], v[26:27], v[94:95] op_sel_hi:[1,0] neg_lo:[0,1] neg_hi:[0,1]
	v_pk_add_f32 v[28:29], v[28:29], v[94:95] op_sel_hi:[1,0] neg_lo:[0,1] neg_hi:[0,1]
	v_add_u32_e32 v109, -1, v107
	v_fma_f32 v110, -v109, v107, v106
	v_cmp_ge_f32_e64 s[8:9], 0, v110
	v_add_u32_e32 v110, 1, v107
	v_pk_add_f32 v[22:23], v[22:23], v[94:95] op_sel_hi:[1,0] neg_lo:[0,1] neg_hi:[0,1]
	v_cndmask_b32_e64 v109, v107, v109, s[8:9]
	v_fma_f32 v107, -v110, v107, v106
	v_cmp_lt_f32_e64 s[8:9], 0, v107
	v_pk_add_f32 v[24:25], v[24:25], v[94:95] op_sel_hi:[1,0] neg_lo:[0,1] neg_hi:[0,1]
	v_pk_add_f32 v[6:7], v[6:7], v[94:95] op_sel_hi:[1,0] neg_lo:[0,1] neg_hi:[0,1]
	v_cndmask_b32_e64 v107, v109, v110, s[8:9]
	v_mul_f32_e32 v109, 0x37800000, v107
	v_cndmask_b32_e64 v107, v107, v109, s[6:7]
	v_cmp_class_f32_e64 s[6:7], v106, v213
	v_add_u32_e32 v110, 0x20300, v147
	v_pk_add_f32 v[8:9], v[8:9], v[94:95] op_sel_hi:[1,0] neg_lo:[0,1] neg_hi:[0,1]
	v_cndmask_b32_e64 v107, v107, v106, s[6:7]
	v_div_scale_f32 v151, s[6:7], v107, v107, 1.0
	v_rcp_f32_e32 v155, v151
	v_div_fmas_f32 v106, v108, v149, v153
	v_div_fixup_f32 v106, v106, v116, 1.0
	v_add_u32_e32 v116, 0x20900, v147
	v_fma_f32 v108, -v151, v155, 1.0
	v_fmac_f32_e32 v155, v108, v155
	v_add_u32_e32 v108, 0x20100, v147
	ds_read_b64 v[108:109], v108
	ds_read_b64 v[110:111], v110
	ds_read_b64 v[112:113], v112
	ds_read_b64 v[114:115], v114
	v_div_scale_f32 v149, vcc, 1.0, v107, 1.0
	s_waitcnt lgkmcnt(3)
	v_pk_add_f32 v[108:109], v[108:109], 0 op_sel_hi:[1,0]
	v_mul_f32_e32 v153, v149, v155
	s_waitcnt lgkmcnt(2)
	v_pk_add_f32 v[108:109], v[108:109], v[110:111]
	s_add_i32 s94, s94, s95
	s_waitcnt lgkmcnt(1)
	v_pk_add_f32 v[108:109], v[108:109], v[112:113]
	ds_read_b64 v[110:111], v116
	ds_read_b64 v[112:113], v117
	ds_read_b64 v[116:117], v157
	ds_read_b64 v[162:163], v159
	s_waitcnt lgkmcnt(4)
	v_pk_add_f32 v[108:109], v[108:109], v[114:115]
	v_add_u32_e32 v157, 0x20780, v147
	s_waitcnt lgkmcnt(3)
	v_pk_add_f32 v[108:109], v[108:109], v[110:111]
	v_add_u32_e32 v159, 0x20980, v147
	s_waitcnt lgkmcnt(2)
	v_pk_add_f32 v[108:109], v[108:109], v[112:113]
	v_fma_f32 v112, -v151, v153, v149
	s_waitcnt lgkmcnt(1)
	v_pk_add_f32 v[108:109], v[108:109], v[116:117]
	v_fmac_f32_e32 v153, v112, v155
	s_waitcnt lgkmcnt(0)
	v_pk_add_f32 v[108:109], v[108:109], v[162:163]
	v_fma_f32 v112, -v151, v153, v149
	v_pk_mul_f32 v[108:109], v[108:109], s[72:73] op_sel_hi:[1,0]
	v_add_u32_e32 v116, 0x20180, v147
	v_fma_f32 v110, -v108, v108, v109
	v_max_f32_e32 v110, 0, v110
	v_add_f32_e32 v110, 0x3727c5ac, v110
	v_mul_f32_e32 v111, 0x4f800000, v110
	v_cmp_gt_f32_e64 s[6:7], s73, v110
	v_add_u32_e32 v117, 0x20380, v147
	v_add_u32_e32 v162, 0x20b80, v147
	v_cndmask_b32_e64 v110, v110, v111, s[6:7]
	v_sqrt_f32_e32 v111, v110
	v_add_u32_e32 v163, 0x20d80, v147
	v_pk_add_f32 v[46:47], v[46:47], v[108:109] op_sel_hi:[1,0] neg_lo:[0,1] neg_hi:[0,1]
	v_pk_add_f32 v[48:49], v[48:49], v[108:109] op_sel_hi:[1,0] neg_lo:[0,1] neg_hi:[0,1]
	v_add_u32_e32 v113, -1, v111
	v_fma_f32 v114, -v113, v111, v110
	v_cmp_ge_f32_e64 s[8:9], 0, v114
	v_add_u32_e32 v114, 1, v111
	v_pk_add_f32 v[42:43], v[42:43], v[108:109] op_sel_hi:[1,0] neg_lo:[0,1] neg_hi:[0,1]
	v_cndmask_b32_e64 v113, v111, v113, s[8:9]
	v_fma_f32 v111, -v114, v111, v110
	v_cmp_lt_f32_e64 s[8:9], 0, v111
	v_pk_add_f32 v[44:45], v[44:45], v[108:109] op_sel_hi:[1,0] neg_lo:[0,1] neg_hi:[0,1]
	v_pk_add_f32 v[38:39], v[38:39], v[108:109] op_sel_hi:[1,0] neg_lo:[0,1] neg_hi:[0,1]
	v_cndmask_b32_e64 v111, v113, v114, s[8:9]
	v_mul_f32_e32 v113, 0x37800000, v111
	v_cndmask_b32_e64 v111, v111, v113, s[6:7]
	v_cmp_class_f32_e64 s[6:7], v110, v213
	v_lshl_add_u64 v[114:115], s[24:25], 0, v[166:167]
	v_pk_add_f32 v[40:41], v[40:41], v[108:109] op_sel_hi:[1,0] neg_lo:[0,1] neg_hi:[0,1]
	v_cndmask_b32_e64 v111, v111, v110, s[6:7]
	v_div_fmas_f32 v110, v112, v155, v153
	v_lshl_add_u64 v[112:113], s[22:23], 0, v[166:167]
	global_load_dwordx4 v[168:171], v[112:113], off
	global_load_dwordx4 v[172:175], v[114:115], off
	v_mov_b32_e32 v252, v166
	global_load_dwordx4 v[236:239], v252, s[22:23] offset:64
	global_load_dwordx4 v[240:243], v252, s[24:25] offset:64
	global_load_dwordx4 v[244:247], v252, s[22:23] offset:128
	global_load_dwordx4 v[248:251], v252, s[24:25] offset:128
	v_add_u32_e32 v155, 0x20580, v147
	ds_read_b64 v[112:113], v116
	ds_read_b64 v[114:115], v117
	ds_read_b64 v[116:117], v155
	ds_read_b64 v[160:161], v157
	v_add_u32_e32 v147, 0x20f80, v147
	s_waitcnt lgkmcnt(3)
	v_pk_add_f32 v[112:113], v[112:113], 0 op_sel_hi:[1,0]
	v_div_scale_f32 v149, s[6:7], v111, v111, 1.0
	s_waitcnt lgkmcnt(2)
	v_pk_add_f32 v[112:113], v[112:113], v[114:115]
	v_rcp_f32_e32 v151, v149
	s_waitcnt lgkmcnt(1)
	v_pk_add_f32 v[112:113], v[112:113], v[116:117]
	ds_read_b64 v[114:115], v159
	ds_read_b64 v[116:117], v162
	ds_read_b64 v[162:163], v163
	ds_read_b64 v[164:165], v147
	s_waitcnt lgkmcnt(4)
	v_pk_add_f32 v[112:113], v[112:113], v[160:161]
	v_div_fixup_f32 v110, v110, v107, 1.0
	s_waitcnt lgkmcnt(3)
	v_pk_add_f32 v[112:113], v[112:113], v[114:115]
	v_fma_f32 v107, -v149, v151, 1.0
	s_waitcnt lgkmcnt(2)
	v_pk_add_f32 v[112:113], v[112:113], v[116:117]
	v_fmac_f32_e32 v151, v107, v151
	s_waitcnt lgkmcnt(1)
	v_pk_add_f32 v[112:113], v[112:113], v[162:163]
	v_div_scale_f32 v107, vcc, 1.0, v111, 1.0
	s_waitcnt lgkmcnt(0)
	v_pk_add_f32 v[112:113], v[112:113], v[164:165]
	v_mul_f32_e32 v153, v107, v151
	v_pk_mul_f32 v[112:113], v[112:113], s[72:73] op_sel_hi:[1,0]
	v_fma_f32 v116, -v149, v153, v107
	v_fma_f32 v114, -v112, v112, v113
	v_max_f32_e32 v114, 0, v114
	v_add_f32_e32 v114, 0x3727c5ac, v114
	v_mul_f32_e32 v115, 0x4f800000, v114
	v_cmp_gt_f32_e64 s[6:7], s73, v114
	v_fmac_f32_e32 v153, v116, v151
	v_fma_f32 v107, -v149, v153, v107
	v_cndmask_b32_e64 v114, v114, v115, s[6:7]
	v_sqrt_f32_e32 v115, v114
	v_div_fmas_f32 v107, v107, v151, v153
	v_or_b32_e32 v160, 16, v176
	v_ashrrev_i32_e32 v161, 31, v160
	v_add_u32_e32 v116, -1, v115
	v_fma_f32 v117, -v116, v115, v114
	v_cmp_ge_f32_e64 s[8:9], 0, v117
	v_add_u32_e32 v117, 1, v115
	v_lshlrev_b64 v[160:161], 12, v[160:161]
	v_cndmask_b32_e64 v116, v115, v116, s[8:9]
	v_fma_f32 v115, -v117, v115, v114
	v_cmp_lt_f32_e64 s[8:9], 0, v115
	v_lshl_add_u64 v[160:161], s[20:21], 0, v[160:161]
	v_or_b32_e32 v164, 32, v176
	v_cndmask_b32_e64 v115, v116, v117, s[8:9]
	v_mul_f32_e32 v116, 0x37800000, v115
	v_cndmask_b32_e64 v115, v115, v116, s[6:7]
	v_cmp_class_f32_e64 s[6:7], v114, v213
	v_lshl_add_u64 v[160:161], v[160:161], 0, v[166:167]
	v_ashrrev_i32_e32 v165, 31, v164
	v_cndmask_b32_e64 v115, v115, v114, s[6:7]
	v_div_scale_f32 v116, s[6:7], v115, v115, 1.0
	v_rcp_f32_e32 v117, v116
	v_div_fixup_f32 v114, v107, v111, 1.0
	v_lshlrev_b64 v[164:165], 12, v[164:165]
	v_lshl_add_u64 v[164:165], s[20:21], 0, v[164:165]
	v_fma_f32 v107, -v116, v117, 1.0
	v_fmac_f32_e32 v117, v107, v117
	v_div_scale_f32 v107, vcc, 1.0, v115, 1.0
	v_mul_f32_e32 v111, v107, v117
	v_fma_f32 v147, -v116, v111, v107
	v_fmac_f32_e32 v111, v147, v117
	v_fma_f32 v107, -v116, v111, v107
	v_div_fmas_f32 v107, v107, v117, v111
	v_lshlrev_b64 v[116:117], 12, v[176:177]
	v_lshl_add_u64 v[116:117], s[20:21], 0, v[116:117]
	v_pk_mul_f32 v[78:79], v[78:79], v[106:107] op_sel_hi:[1,0]
	v_pk_mul_f32 v[80:81], v[80:81], v[106:107] op_sel_hi:[1,0]
	v_lshl_add_u64 v[116:117], v[116:117], 0, v[166:167]
	v_or_b32_e32 v176, 48, v176
	v_ashrrev_i32_e32 v177, 31, v176
	v_div_fixup_f32 v162, v107, v115, 1.0
	v_lshlrev_b64 v[176:177], 12, v[176:177]
	v_pk_add_f32 v[142:143], v[142:143], v[112:113] op_sel_hi:[1,0] neg_lo:[0,1] neg_hi:[0,1]
	v_pk_add_f32 v[144:145], v[144:145], v[112:113] op_sel_hi:[1,0] neg_lo:[0,1] neg_hi:[0,1]
	s_waitcnt vmcnt(4)
	v_pk_fma_f32 v[78:79], v[78:79], v[168:169], v[172:173]
	v_pk_fma_f32 v[80:81], v[80:81], v[170:171], v[174:175]
	global_store_dwordx4 v[116:117], v[78:81], off
	v_lshl_add_u64 v[164:165], v[164:165], 0, v[166:167]
	v_lshl_add_u64 v[176:177], s[20:21], 0, v[176:177]
	v_pk_add_f32 v[78:79], v[98:99], v[96:97] op_sel_hi:[1,0] neg_lo:[0,1] neg_hi:[0,1]
	v_pk_add_f32 v[80:81], v[100:101], v[96:97] op_sel_hi:[1,0] neg_lo:[0,1] neg_hi:[0,1]
	v_pk_mul_f32 v[78:79], v[78:79], v[110:111] op_sel_hi:[1,0]
	v_pk_mul_f32 v[80:81], v[80:81], v[110:111] op_sel_hi:[1,0]
	v_pk_fma_f32 v[78:79], v[78:79], v[168:169], v[172:173]
	v_pk_fma_f32 v[80:81], v[80:81], v[170:171], v[174:175]
	global_store_dwordx4 v[160:161], v[78:81], off
	v_pk_mul_f32 v[142:143], v[142:143], v[162:163] op_sel_hi:[1,0]
	v_pk_mul_f32 v[144:145], v[144:145], v[162:163] op_sel_hi:[1,0]
	v_pk_add_f32 v[78:79], v[126:127], v[108:109] op_sel_hi:[1,0] neg_lo:[0,1] neg_hi:[0,1]
	v_pk_add_f32 v[80:81], v[128:129], v[108:109] op_sel_hi:[1,0] neg_lo:[0,1] neg_hi:[0,1]
	v_pk_mul_f32 v[78:79], v[78:79], v[114:115] op_sel_hi:[1,0]
	v_pk_mul_f32 v[80:81], v[80:81], v[114:115] op_sel_hi:[1,0]
	v_pk_fma_f32 v[78:79], v[78:79], v[168:169], v[172:173]
	v_pk_fma_f32 v[80:81], v[80:81], v[170:171], v[174:175]
	v_ashrrev_i32_e32 v159, 31, v158
	v_lshl_add_u64 v[166:167], v[176:177], 0, v[166:167]
	v_pk_fma_f32 v[142:143], v[168:169], v[142:143], v[172:173]
	v_pk_fma_f32 v[144:145], v[170:171], v[144:145], v[174:175]
	global_store_dwordx4 v[164:165], v[78:81], off
	global_store_dwordx4 v[166:167], v[142:145], off
	v_pk_mul_f32 v[70:71], v[70:71], v[106:107] op_sel_hi:[1,0]
	v_lshlrev_b64 v[78:79], 2, v[158:159]
	v_lshl_add_u64 v[80:81], s[22:23], 0, v[78:79]
	v_lshl_add_u64 v[98:99], s[24:25], 0, v[78:79]
	s_nop 0
	v_pk_mul_f32 v[72:73], v[72:73], v[106:107] op_sel_hi:[1,0]
	v_pk_add_f32 v[126:127], v[138:139], v[112:113] op_sel_hi:[1,0] neg_lo:[0,1] neg_hi:[0,1]
	v_pk_add_f32 v[128:129], v[140:141], v[112:113] op_sel_hi:[1,0] neg_lo:[0,1] neg_hi:[0,1]
	v_pk_mul_f32 v[126:127], v[126:127], v[162:163] op_sel_hi:[1,0]
	v_pk_mul_f32 v[128:129], v[128:129], v[162:163] op_sel_hi:[1,0]
	v_ashrrev_i32_e32 v157, 31, v156
	v_pk_mul_f32 v[62:63], v[62:63], v[106:107] op_sel_hi:[1,0]
	v_pk_mul_f32 v[64:65], v[64:65], v[106:107] op_sel_hi:[1,0]
	v_ashrrev_i32_e32 v155, 31, v154
	v_pk_mul_f32 v[54:55], v[54:55], v[106:107] op_sel_hi:[1,0]
	v_pk_mul_f32 v[56:57], v[56:57], v[106:107] op_sel_hi:[1,0]
	v_ashrrev_i32_e32 v153, 31, v152
	v_pk_mul_f32 v[58:59], v[58:59], v[106:107] op_sel_hi:[1,0]
	v_pk_mul_f32 v[60:61], v[60:61], v[106:107] op_sel_hi:[1,0]
	v_pk_add_f32 v[18:19], v[18:19], v[112:113] op_sel_hi:[1,0] neg_lo:[0,1] neg_hi:[0,1]
	v_pk_add_f32 v[20:21], v[20:21], v[112:113] op_sel_hi:[1,0] neg_lo:[0,1] neg_hi:[0,1]
	v_pk_mul_f32 v[18:19], v[18:19], v[162:163] op_sel_hi:[1,0]
	v_pk_mul_f32 v[46:47], v[46:47], v[114:115] op_sel_hi:[1,0]
	v_pk_mul_f32 v[48:49], v[48:49], v[114:115] op_sel_hi:[1,0]
	v_pk_mul_f32 v[20:21], v[20:21], v[162:163] op_sel_hi:[1,0]
	v_ashrrev_i32_e32 v151, 31, v150
	v_pk_add_f32 v[14:15], v[14:15], v[112:113] op_sel_hi:[1,0] neg_lo:[0,1] neg_hi:[0,1]
	v_pk_add_f32 v[16:17], v[16:17], v[112:113] op_sel_hi:[1,0] neg_lo:[0,1] neg_hi:[0,1]
	v_pk_mul_f32 v[26:27], v[26:27], v[106:107] op_sel_hi:[1,0]
	v_pk_mul_f32 v[28:29], v[28:29], v[106:107] op_sel_hi:[1,0]
	v_ashrrev_i32_e32 v149, 31, v148
	v_pk_mul_f32 v[14:15], v[14:15], v[162:163] op_sel_hi:[1,0]
	v_pk_mul_f32 v[16:17], v[16:17], v[162:163] op_sel_hi:[1,0]
	v_ashrrev_i32_e32 v147, 31, v146
	v_pk_add_f32 v[10:11], v[10:11], v[112:113] op_sel_hi:[1,0] neg_lo:[0,1] neg_hi:[0,1]
	v_pk_add_f32 v[12:13], v[12:13], v[112:113] op_sel_hi:[1,0] neg_lo:[0,1] neg_hi:[0,1]
	v_pk_mul_f32 v[22:23], v[22:23], v[106:107] op_sel_hi:[1,0]
	v_pk_mul_f32 v[24:25], v[24:25], v[106:107] op_sel_hi:[1,0]
	v_pk_mul_f32 v[38:39], v[38:39], v[114:115] op_sel_hi:[1,0]
	v_pk_mul_f32 v[40:41], v[40:41], v[114:115] op_sel_hi:[1,0]
	v_pk_mul_f32 v[10:11], v[10:11], v[162:163] op_sel_hi:[1,0]
	v_pk_mul_f32 v[12:13], v[12:13], v[162:163] op_sel_hi:[1,0]
	v_pk_add_f32 v[2:3], v[2:3], v[112:113] op_sel_hi:[1,0] neg_lo:[0,1] neg_hi:[0,1]
	v_pk_add_f32 v[4:5], v[4:5], v[112:113] op_sel_hi:[1,0] neg_lo:[0,1] neg_hi:[0,1]
	v_pk_mul_f32 v[6:7], v[6:7], v[106:107] op_sel_hi:[1,0]
	v_pk_mul_f32 v[8:9], v[8:9], v[106:107] op_sel_hi:[1,0]
	v_pk_mul_f32 v[2:3], v[2:3], v[162:163] op_sel_hi:[1,0]
	v_pk_mul_f32 v[4:5], v[4:5], v[162:163] op_sel_hi:[1,0]
	v_readlane_b32 s6, v254, 0
	s_add_i32 s96, s96, s97
	s_waitcnt vmcnt(6)
	v_pk_fma_f32 v[70:71], v[70:71], v[236:237], v[240:241]
	v_pk_fma_f32 v[72:73], v[72:73], v[238:239], v[242:243]
	global_store_dwordx4 v[116:117], v[70:73], off offset:64
	v_pk_fma_f32 v[126:127], v[126:127], v[236:237], v[240:241]
	v_pk_fma_f32 v[128:129], v[128:129], v[238:239], v[242:243]
	v_pk_add_f32 v[70:71], v[90:91], v[96:97] op_sel_hi:[1,0] neg_lo:[0,1] neg_hi:[0,1]
	v_pk_add_f32 v[72:73], v[92:93], v[96:97] op_sel_hi:[1,0] neg_lo:[0,1] neg_hi:[0,1]
	v_pk_mul_f32 v[70:71], v[70:71], v[110:111] op_sel_hi:[1,0]
	v_pk_mul_f32 v[72:73], v[72:73], v[110:111] op_sel_hi:[1,0]
	v_pk_fma_f32 v[70:71], v[70:71], v[236:237], v[240:241]
	v_pk_fma_f32 v[72:73], v[72:73], v[238:239], v[242:243]
	global_store_dwordx4 v[160:161], v[70:73], off offset:64
	v_pk_add_f32 v[90:91], v[134:135], v[112:113] op_sel_hi:[1,0] neg_lo:[0,1] neg_hi:[0,1]
	v_pk_add_f32 v[92:93], v[136:137], v[112:113] op_sel_hi:[1,0] neg_lo:[0,1] neg_hi:[0,1]
	v_pk_add_f32 v[70:71], v[122:123], v[108:109] op_sel_hi:[1,0] neg_lo:[0,1] neg_hi:[0,1]
	v_pk_add_f32 v[72:73], v[124:125], v[108:109] op_sel_hi:[1,0] neg_lo:[0,1] neg_hi:[0,1]
	v_pk_mul_f32 v[70:71], v[70:71], v[114:115] op_sel_hi:[1,0]
	v_pk_mul_f32 v[72:73], v[72:73], v[114:115] op_sel_hi:[1,0]
	v_pk_fma_f32 v[70:71], v[70:71], v[236:237], v[240:241]
	v_pk_fma_f32 v[72:73], v[72:73], v[238:239], v[242:243]
	global_store_dwordx4 v[164:165], v[70:73], off offset:64
	global_store_dwordx4 v[166:167], v[126:129], off offset:64
	global_load_dwordx4 v[236:239], v252, s[22:23] offset:192
	global_load_dwordx4 v[240:243], v252, s[24:25] offset:192
	v_pk_mul_f32 v[90:91], v[90:91], v[162:163] op_sel_hi:[1,0]
	v_lshlrev_b64 v[70:71], 2, v[156:157]
	v_lshl_add_u64 v[72:73], s[22:23], 0, v[70:71]
	v_lshl_add_u64 v[78:79], s[24:25], 0, v[70:71]
	s_nop 0
	v_pk_mul_f32 v[92:93], v[92:93], v[162:163] op_sel_hi:[1,0]
	s_waitcnt vmcnt(10)
	v_pk_fma_f32 v[62:63], v[62:63], v[244:245], v[248:249]
	v_pk_fma_f32 v[64:65], v[64:65], v[246:247], v[250:251]
	global_store_dwordx4 v[116:117], v[62:65], off offset:128
	v_pk_fma_f32 v[90:91], v[90:91], v[244:245], v[248:249]
	v_pk_fma_f32 v[92:93], v[92:93], v[246:247], v[250:251]
	v_pk_add_f32 v[62:63], v[86:87], v[96:97] op_sel_hi:[1,0] neg_lo:[0,1] neg_hi:[0,1]
	v_pk_add_f32 v[64:65], v[88:89], v[96:97] op_sel_hi:[1,0] neg_lo:[0,1] neg_hi:[0,1]
	v_pk_mul_f32 v[62:63], v[62:63], v[110:111] op_sel_hi:[1,0]
	v_pk_mul_f32 v[64:65], v[64:65], v[110:111] op_sel_hi:[1,0]
	v_pk_fma_f32 v[62:63], v[62:63], v[244:245], v[248:249]
	v_pk_fma_f32 v[64:65], v[64:65], v[246:247], v[250:251]
	global_store_dwordx4 v[160:161], v[62:65], off offset:128
	s_nop 1
	v_pk_add_f32 v[62:63], v[118:119], v[108:109] op_sel_hi:[1,0] neg_lo:[0,1] neg_hi:[0,1]
	v_pk_add_f32 v[64:65], v[120:121], v[108:109] op_sel_hi:[1,0] neg_lo:[0,1] neg_hi:[0,1]
	v_pk_mul_f32 v[62:63], v[62:63], v[114:115] op_sel_hi:[1,0]
	v_pk_mul_f32 v[64:65], v[64:65], v[114:115] op_sel_hi:[1,0]
	v_pk_fma_f32 v[62:63], v[62:63], v[244:245], v[248:249]
	v_pk_fma_f32 v[64:65], v[64:65], v[246:247], v[250:251]
	global_store_dwordx4 v[164:165], v[62:65], off offset:128
	global_store_dwordx4 v[166:167], v[90:93], off offset:128
	global_load_dwordx4 v[244:247], v252, s[22:23] offset:256
	global_load_dwordx4 v[248:251], v252, s[24:25] offset:256
	v_pk_add_f32 v[78:79], v[130:131], v[112:113] op_sel_hi:[1,0] neg_lo:[0,1] neg_hi:[0,1]
	v_lshlrev_b64 v[62:63], 2, v[154:155]
	v_lshl_add_u64 v[64:65], s[22:23], 0, v[62:63]
	v_lshl_add_u64 v[70:71], s[24:25], 0, v[62:63]
	s_nop 0
	v_pk_add_f32 v[80:81], v[132:133], v[112:113] op_sel_hi:[1,0] neg_lo:[0,1] neg_hi:[0,1]
	v_pk_mul_f32 v[78:79], v[78:79], v[162:163] op_sel_hi:[1,0]
	v_pk_mul_f32 v[80:81], v[80:81], v[162:163] op_sel_hi:[1,0]
	s_waitcnt vmcnt(6)
	v_pk_fma_f32 v[54:55], v[54:55], v[236:237], v[240:241]
	v_pk_fma_f32 v[56:57], v[56:57], v[238:239], v[242:243]
	global_store_dwordx4 v[116:117], v[54:57], off offset:192
	v_pk_fma_f32 v[78:79], v[78:79], v[236:237], v[240:241]
	v_pk_fma_f32 v[80:81], v[80:81], v[238:239], v[242:243]
	v_pk_add_f32 v[54:55], v[82:83], v[96:97] op_sel_hi:[1,0] neg_lo:[0,1] neg_hi:[0,1]
	v_pk_add_f32 v[56:57], v[84:85], v[96:97] op_sel_hi:[1,0] neg_lo:[0,1] neg_hi:[0,1]
	v_pk_mul_f32 v[54:55], v[54:55], v[110:111] op_sel_hi:[1,0]
	v_pk_mul_f32 v[56:57], v[56:57], v[110:111] op_sel_hi:[1,0]
	v_pk_fma_f32 v[54:55], v[54:55], v[236:237], v[240:241]
	v_pk_fma_f32 v[56:57], v[56:57], v[238:239], v[242:243]
	global_store_dwordx4 v[160:161], v[54:57], off offset:192
	s_nop 1
	v_pk_add_f32 v[54:55], v[102:103], v[108:109] op_sel_hi:[1,0] neg_lo:[0,1] neg_hi:[0,1]
	v_pk_add_f32 v[56:57], v[104:105], v[108:109] op_sel_hi:[1,0] neg_lo:[0,1] neg_hi:[0,1]
	v_pk_mul_f32 v[54:55], v[54:55], v[114:115] op_sel_hi:[1,0]
	v_pk_mul_f32 v[56:57], v[56:57], v[114:115] op_sel_hi:[1,0]
	v_pk_fma_f32 v[54:55], v[54:55], v[236:237], v[240:241]
	v_pk_fma_f32 v[56:57], v[56:57], v[238:239], v[242:243]
	global_store_dwordx4 v[164:165], v[54:57], off offset:192
	global_store_dwordx4 v[166:167], v[78:81], off offset:192
	global_load_dwordx4 v[236:239], v252, s[22:23] offset:320
	global_load_dwordx4 v[240:243], v252, s[24:25] offset:320
	v_pk_add_f32 v[70:71], v[74:75], v[96:97] op_sel_hi:[1,0] neg_lo:[0,1] neg_hi:[0,1]
	v_lshlrev_b64 v[54:55], 2, v[152:153]
	v_lshl_add_u64 v[56:57], s[22:23], 0, v[54:55]
	v_lshl_add_u64 v[62:63], s[24:25], 0, v[54:55]
	s_nop 0
	s_waitcnt vmcnt(6)
	v_pk_fma_f32 v[58:59], v[58:59], v[244:245], v[248:249]
	v_pk_fma_f32 v[60:61], v[60:61], v[246:247], v[250:251]
	global_store_dwordx4 v[116:117], v[58:61], off offset:256
	v_pk_fma_f32 v[18:19], v[18:19], v[244:245], v[248:249]
	v_pk_fma_f32 v[46:47], v[46:47], v[244:245], v[248:249]
	v_pk_add_f32 v[60:61], v[76:77], v[96:97] op_sel_hi:[1,0] neg_lo:[0,1] neg_hi:[0,1]
	v_pk_mul_f32 v[58:59], v[70:71], v[110:111] op_sel_hi:[1,0]
	v_pk_mul_f32 v[60:61], v[60:61], v[110:111] op_sel_hi:[1,0]
	v_pk_fma_f32 v[58:59], v[58:59], v[244:245], v[248:249]
	v_pk_fma_f32 v[60:61], v[60:61], v[246:247], v[250:251]
	v_pk_fma_f32 v[48:49], v[48:49], v[246:247], v[250:251]
	v_pk_fma_f32 v[20:21], v[20:21], v[246:247], v[250:251]
	global_store_dwordx4 v[160:161], v[58:61], off offset:256
	global_store_dwordx4 v[164:165], v[46:49], off offset:256
	global_store_dwordx4 v[166:167], v[18:21], off offset:256
	global_load_dwordx4 v[244:247], v252, s[22:23] offset:384
	global_load_dwordx4 v[248:251], v252, s[24:25] offset:384
	v_pk_add_f32 v[58:59], v[66:67], v[96:97] op_sel_hi:[1,0] neg_lo:[0,1] neg_hi:[0,1]
	v_pk_add_f32 v[60:61], v[68:69], v[96:97] op_sel_hi:[1,0] neg_lo:[0,1] neg_hi:[0,1]
	v_lshlrev_b64 v[18:19], 2, v[150:151]
	v_lshl_add_u64 v[20:21], s[22:23], 0, v[18:19]
	v_lshl_add_u64 v[46:47], s[24:25], 0, v[18:19]
	s_nop 0
	v_pk_mul_f32 v[58:59], v[58:59], v[110:111] op_sel_hi:[1,0]
	v_pk_mul_f32 v[60:61], v[60:61], v[110:111] op_sel_hi:[1,0]
	v_pk_mul_f32 v[62:63], v[42:43], v[114:115] op_sel_hi:[1,0]
	v_pk_mul_f32 v[64:65], v[44:45], v[114:115] op_sel_hi:[1,0]
	v_lshlrev_b64 v[54:55], 2, v[148:149]
	v_lshl_add_u64 v[56:57], s[22:23], 0, v[54:55]
	v_lshl_add_u64 v[54:55], s[24:25], 0, v[54:55]
	s_waitcnt vmcnt(6)
	v_pk_fma_f32 v[26:27], v[26:27], v[236:237], v[240:241]
	v_pk_fma_f32 v[28:29], v[28:29], v[238:239], v[242:243]
	v_pk_fma_f32 v[14:15], v[14:15], v[236:237], v[240:241]
	v_pk_fma_f32 v[16:17], v[16:17], v[238:239], v[242:243]
	v_pk_fma_f32 v[42:43], v[58:59], v[236:237], v[240:241]
	v_pk_fma_f32 v[44:45], v[60:61], v[238:239], v[242:243]
	v_pk_fma_f32 v[18:19], v[62:63], v[236:237], v[240:241]
	v_pk_fma_f32 v[20:21], v[64:65], v[238:239], v[242:243]
	global_store_dwordx4 v[116:117], v[26:29], off offset:320
	global_store_dwordx4 v[160:161], v[42:45], off offset:320
	global_store_dwordx4 v[164:165], v[18:21], off offset:320
	global_store_dwordx4 v[166:167], v[14:17], off offset:320
	global_load_dwordx4 v[236:239], v252, s[22:23] offset:448
	global_load_dwordx4 v[240:243], v252, s[24:25] offset:448
	v_lshlrev_b64 v[26:27], 2, v[146:147]
	v_lshl_add_u64 v[42:43], s[22:23], 0, v[26:27]
	v_lshl_add_u64 v[44:45], s[24:25], 0, v[26:27]
	v_pk_add_f32 v[26:27], v[50:51], v[96:97] op_sel_hi:[1,0] neg_lo:[0,1] neg_hi:[0,1]
	v_pk_add_f32 v[28:29], v[52:53], v[96:97] op_sel_hi:[1,0] neg_lo:[0,1] neg_hi:[0,1]
	v_pk_mul_f32 v[26:27], v[26:27], v[110:111] op_sel_hi:[1,0]
	v_pk_mul_f32 v[28:29], v[28:29], v[110:111] op_sel_hi:[1,0]
	s_waitcnt vmcnt(6)
	v_pk_fma_f32 v[22:23], v[22:23], v[244:245], v[248:249]
	v_pk_fma_f32 v[24:25], v[24:25], v[246:247], v[250:251]
	v_pk_fma_f32 v[10:11], v[10:11], v[244:245], v[248:249]
	v_pk_fma_f32 v[12:13], v[12:13], v[246:247], v[250:251]
	v_pk_fma_f32 v[26:27], v[26:27], v[244:245], v[248:249]
	v_pk_fma_f32 v[28:29], v[28:29], v[246:247], v[250:251]
	v_pk_fma_f32 v[14:15], v[38:39], v[244:245], v[248:249]
	v_pk_fma_f32 v[16:17], v[40:41], v[246:247], v[250:251]
	global_store_dwordx4 v[116:117], v[22:25], off offset:384
	global_store_dwordx4 v[160:161], v[26:29], off offset:384
	global_store_dwordx4 v[164:165], v[14:17], off offset:384
	global_store_dwordx4 v[166:167], v[10:13], off offset:384
	s_load_dword s7, s[0:1], 0x150
	v_pk_add_f32 v[18:19], v[30:31], v[96:97] op_sel_hi:[1,0] neg_lo:[0,1] neg_hi:[0,1]
	v_pk_add_f32 v[20:21], v[32:33], v[96:97] op_sel_hi:[1,0] neg_lo:[0,1] neg_hi:[0,1]
	v_pk_add_f32 v[22:23], v[34:35], v[108:109] op_sel_hi:[1,0] neg_lo:[0,1] neg_hi:[0,1]
	v_pk_add_f32 v[24:25], v[36:37], v[108:109] op_sel_hi:[1,0] neg_lo:[0,1] neg_hi:[0,1]
	v_pk_mul_f32 v[18:19], v[18:19], v[110:111] op_sel_hi:[1,0]
	v_pk_mul_f32 v[20:21], v[20:21], v[110:111] op_sel_hi:[1,0]
	v_pk_mul_f32 v[22:23], v[22:23], v[114:115] op_sel_hi:[1,0]
	v_pk_mul_f32 v[24:25], v[24:25], v[114:115] op_sel_hi:[1,0]
	s_waitcnt lgkmcnt(0)
	s_add_i32 s6, s6, s7
	v_writelane_b32 v254, s6, 0
	s_cmpk_gt_i32 s6, 0xff
	s_waitcnt vmcnt(4)
	v_pk_fma_f32 v[6:7], v[6:7], v[236:237], v[240:241]
	v_pk_fma_f32 v[8:9], v[8:9], v[238:239], v[242:243]
	v_pk_fma_f32 v[2:3], v[2:3], v[236:237], v[240:241]
	v_pk_fma_f32 v[4:5], v[4:5], v[238:239], v[242:243]
	v_pk_fma_f32 v[18:19], v[18:19], v[236:237], v[240:241]
	v_pk_fma_f32 v[20:21], v[20:21], v[238:239], v[242:243]
	v_pk_fma_f32 v[10:11], v[22:23], v[236:237], v[240:241]
	v_pk_fma_f32 v[12:13], v[24:25], v[238:239], v[242:243]
	global_store_dwordx4 v[116:117], v[6:9], off offset:448
	global_store_dwordx4 v[160:161], v[18:21], off offset:448
	global_store_dwordx4 v[164:165], v[10:13], off offset:448
	global_store_dwordx4 v[166:167], v[2:5], off offset:448
	s_barrier
	s_cbranch_scc1 .LBB0_1109
